# P11 sweep U: per-batch gelu/gate evaluation deferred to the between-sweeps step (2 picks per lane, once per token); scan loader LDS writes interleaved with next loads; scan compute S-pack moved into M
# speedup vs baseline: 1.0386x; 1.0173x over previous
; __device__ __forceinline__ void gdn_scan(const Params& P, LAS unsigned char* lds, int sb, int tid, int lane, int wave) {
;     ...
;     f32x4 S[8];
; #pragma unroll
;     for (int i = 0; i < 8; ++i) S[i] = (f32x4){0.f, 0.f, 0.f, 0.f};
;     SC_BAR();
; #pragma unroll 1
;     for (int n2 = 0; n2 < NCH; ++n2) {
;         if (SCAN_REPS > 1 && (n2 & 127) == 0) {
; #pragma unroll
;             for (int i = 0; i < 8; ++i) S[i] = (f32x4){0.f, 0.f, 0.f, 0.f};
;         }
;         if (SCAN_EXP == 2 && n2 < 128) { SC_BAR(); continue; }
;         const int par = n2 & 1;
;         LAS unsigned char* buf = lds + par * SC_BUF;
;         bf16x8 fA[16], fB[16], fC[16], fD[8];
; #pragma unroll
;         for (int rho = 0; rho < 4; ++rho)
; #pragma unroll
;             for (int s = 0; s < 4; ++s) fA[rho * 4 + s] = *(const LAS bf16x8*)(buf + SC_WN + (16 * rho + col) * 272 + (32 * s + 8 * g) * 2);
; #pragma unroll
;         for (int rho = 0; rho < 4; ++rho)
; #pragma unroll
;             for (int s = 0; s < 4; ++s) fB[rho * 4 + s] = *(const LAS bf16x8*)(buf + SC_QD + (16 * rho + col) * 272 + (32 * s + 8 * g) * 2);
;         const LAS v4u* ufp = (const LAS v4u*)(lds + SC_UFS + par * (SCAN_NWC * 2048) + wave * 2048 + lane * 32);
;         const v4u uf0 = ufp[0], uf1 = ufp[1];
;         const float dec = ((const LAS float*)(lds + SC_DECS))[n2 & 127];
;         bf16x8 Bs[4];
; #pragma unroll
;         for (int s = 0; s < 4; ++s) Bs[s] = pack_b(S[2 * s], S[2 * s + 1]);
;         f32x4 Vn[4], Oc[4];
;         Vn[0] = (f32x4){bflo(uf0.x), bfhi(uf0.x), bflo(uf0.y), bfhi(uf0.y)}; Vn[1] = (f32x4){bflo(uf0.z), bfhi(uf0.z), bflo(uf0.w), bfhi(uf0.w)};
;         Vn[2] = (f32x4){bflo(uf1.x), bfhi(uf1.x), bflo(uf1.y), bfhi(uf1.y)}; Vn[3] = (f32x4){bflo(uf1.z), bfhi(uf1.z), bflo(uf1.w), bfhi(uf1.w)};
;         __builtin_amdgcn_sched_barrier(0);
;         PIN16(fA);
; #pragma unroll
;         for (int s = 0; s < 4; ++s)
; #pragma unroll
;             for (int rho = 0; rho < 4; ++rho) Vn[rho] = __builtin_amdgcn_mfma_f32_16x16x32_bf16(fA[rho * 4 + s], Bs[s], Vn[rho], 0, 0, 0);
;         __builtin_amdgcn_sched_barrier(0);
; #pragma unroll
;         for (int tau = 0; tau < 8; ++tau)
; #pragma unroll
;             for (int s = 0; s < 2; ++s) fC[tau * 2 + s] = *(const LAS bf16x8*)(buf + SC_KD + (16 * tau + col) * 144 + (32 * s + 8 * g) * 2);
;         __builtin_amdgcn_sched_barrier(0);
;         PIN16(fB);
.LBB0_2144:
	v_readlane_b32 s4, v254, 56
	s_lshl_b32 s3, s4, 11
	s_add_i32 s3, s3, 0
	v_lshrrev_b32_e32 v2, 2, v182
	s_add_i32 s3, s3, 0x1e800
	v_and_b32_e32 v3, 12, v2
	v_lshl_add_u32 v1, v182, 5, s3
	s_and_b32 s3, s74, 0xc0
	v_mul_u32_u24_e32 v41, 0x90, v3
	v_or_b32_e32 v3, 3, v2
	s_add_i32 s3, s3, 0
	v_mul_u32_u24_e32 v42, 0x90, v3
	v_or_b32_e32 v3, 19, v2
	s_waitcnt lgkmcnt(0)
	s_barrier
	v_readlane_b32 s5, v254, 57
	s_add_i32 s3, s3, 0x20a00
	v_or_b32_e32 v4, 0x70, v182
	v_mul_u32_u24_e32 v43, 0x90, v3
	v_or_b32_e32 v3, 35, v2
	v_or_b32_e32 v2, 51, v2
	s_mov_b32 s1, 0
	v_lshl_add_u32 v35, v142, 2, s3
	v_mul_u32_u24_e32 v36, 0x110, v142
	v_mul_u32_u24_e32 v37, 0x110, v143
	v_mul_u32_u24_e32 v38, 0x90, v142
	v_mul_u32_u24_e32 v39, 0x90, v143
	v_mul_u32_u24_e32 v40, 0x90, v4
	v_mul_u32_u24_e32 v44, 0x90, v3
	v_mul_u32_u24_e32 v45, 0x90, v2
	s_add_i32 s3, 0, 0x20800
	v_add_u32_e32 v46, 0, v141
	v_mov_b32_e32 v2, 0
	v_mov_b32_e32 v3, 0
	v_mov_b32_e32 v4, 0
	v_mov_b32_e32 v5, 0
	v_mov_b32_e32 v6, 0
	v_mov_b32_e32 v7, 0
	v_mov_b32_e32 v8, 0
	v_mov_b32_e32 v9, 0
	v_mov_b32_e32 v10, 0
	v_mov_b32_e32 v11, 0
	v_mov_b32_e32 v12, 0
	v_mov_b32_e32 v13, 0
	v_mov_b32_e32 v14, 0
	v_mov_b32_e32 v15, 0
	v_mov_b32_e32 v16, 0
	v_mov_b32_e32 v17, 0
	v_mov_b32_e32 v18, 0
	v_mov_b32_e32 v19, 0
	v_mov_b32_e32 v20, 0
	v_mov_b32_e32 v21, 0
	v_mov_b32_e32 v22, 0
	v_mov_b32_e32 v23, 0
	v_mov_b32_e32 v24, 0
	v_mov_b32_e32 v25, 0
	v_mov_b32_e32 v26, 0
	v_mov_b32_e32 v27, 0
	v_mov_b32_e32 v28, 0
	v_mov_b32_e32 v29, 0
	v_mov_b32_e32 v30, 0
	v_mov_b32_e32 v31, 0
	v_mov_b32_e32 v32, 0
	v_mov_b32_e32 v33, 0
	s_movk_i32 s4, 0x7fff
	s_mov_b32 s5, 0xffff0000
	v_mov_b32_e32 v212, 0
	v_mov_b32_e32 v213, 0
	v_mov_b32_e32 v214, 0
	v_mov_b32_e32 v215, 0
	v_mov_b32_e32 v216, 0
	v_mov_b32_e32 v217, 0
	v_mov_b32_e32 v218, 0
	v_mov_b32_e32 v219, 0
	v_mov_b32_e32 v220, 0
	v_mov_b32_e32 v221, 0
	v_mov_b32_e32 v222, 0
	v_mov_b32_e32 v223, 0
	v_mov_b32_e32 v224, 0
	v_mov_b32_e32 v225, 0
	v_mov_b32_e32 v226, 0
	v_mov_b32_e32 v227, 0
.LBB0_2145:
	s_and_b32 s6, s1, 1
	s_mul_i32 s7, s6, 0xf400
	v_add_u32_e32 v47, s7, v46
	v_lshl_add_u32 v34, s6, 12, v1
	v_add_u32_e32 v158, v47, v37
	ds_read_b128 v[48:51], v34
	ds_read_b128 v[52:55], v34 offset:16
	v_mov_b32_e32 v34, s3
	v_add_u32_e32 v141, v47, v36
	ds_read_b32 v34, v34
	ds_read_b128 v[80:83], v158 offset:192
	ds_read_b128 v[84:87], v158 offset:128
	ds_read_b128 v[88:91], v158 offset:64
	ds_read_b128 v[92:95], v158
	ds_read_b128 v[96:99], v141 offset:8896
	ds_read_b128 v[100:103], v141 offset:8832
	ds_read_b128 v[104:107], v141 offset:8768
	ds_read_b128 v[108:111], v141 offset:8704
	ds_read_b128 v[112:115], v141 offset:4544
	ds_read_b128 v[116:119], v141 offset:4480
	ds_read_b128 v[120:123], v141 offset:4416
	ds_read_b128 v[124:127], v141 offset:4352
	ds_read_b128 v[128:131], v141 offset:192
	ds_read_b128 v[132:135], v141 offset:128
	ds_read_b128 v[136:139], v141 offset:64
	ds_read_b128 v[142:145], v141
	ds_read_b128 v[146:149], v158 offset:17600
	ds_read_b128 v[150:153], v158 offset:17536
	ds_read_b128 v[154:157], v158 offset:17472
	ds_read_b128 v[158:161], v158 offset:17408
	ds_read_b128 v[162:165], v141 offset:26304
	ds_read_b128 v[166:169], v141 offset:26240
	ds_read_b128 v[170:173], v141 offset:26176
	ds_read_b128 v[174:177], v141 offset:26112
	ds_read_b128 v[178:181], v141 offset:21952
	ds_read_b128 v[184:187], v141 offset:21888
	ds_read_b128 v[188:191], v141 offset:21824
	ds_read_b128 v[192:195], v141 offset:21760
	ds_read_b128 v[196:199], v141 offset:17600
	ds_read_b128 v[200:203], v141 offset:17536
	ds_read_b128 v[204:207], v141 offset:17472
	ds_read_b128 v[208:211], v141 offset:17408
	s_waitcnt lgkmcnt(15)
	v_lshlrev_b32_e32 v72, 16, v48
	v_and_b32_e32 v73, 0xffff0000, v48
	v_lshlrev_b32_e32 v74, 16, v49
	v_and_b32_e32 v75, 0xffff0000, v49
	v_lshlrev_b32_e32 v48, 16, v50
	v_and_b32_e32 v49, 0xffff0000, v50
	v_lshlrev_b32_e32 v50, 16, v51
	v_and_b32_e32 v51, 0xffff0000, v51
	v_lshlrev_b32_e32 v76, 16, v52
	v_and_b32_e32 v77, 0xffff0000, v52
	v_lshlrev_b32_e32 v78, 16, v53
	v_and_b32_e32 v79, 0xffff0000, v53
	v_lshlrev_b32_e32 v52, 16, v54
	v_and_b32_e32 v53, 0xffff0000, v54
	v_lshlrev_b32_e32 v54, 16, v55
	v_and_b32_e32 v55, 0xffff0000, v55
	s_nop 0
	v_mfma_f32_16x16x32_bf16 v[72:75], v[142:145], v[212:215], v[72:75]
	v_mfma_f32_16x16x32_bf16 v[48:51], v[124:127], v[212:215], v[48:51]
	v_mfma_f32_16x16x32_bf16 v[76:79], v[108:111], v[212:215], v[76:79]
	v_mfma_f32_16x16x32_bf16 v[52:55], v[92:95], v[212:215], v[52:55]
	v_mfma_f32_16x16x32_bf16 v[72:75], v[136:139], v[216:219], v[72:75]
	v_mfma_f32_16x16x32_bf16 v[48:51], v[120:123], v[216:219], v[48:51]
	v_mfma_f32_16x16x32_bf16 v[76:79], v[104:107], v[216:219], v[76:79]
	v_mfma_f32_16x16x32_bf16 v[52:55], v[88:91], v[216:219], v[52:55]
	v_mfma_f32_16x16x32_bf16 v[72:75], v[132:135], v[220:223], v[72:75]
	v_mfma_f32_16x16x32_bf16 v[48:51], v[116:119], v[220:223], v[48:51]
	v_mfma_f32_16x16x32_bf16 v[76:79], v[100:103], v[220:223], v[76:79]
	v_mfma_f32_16x16x32_bf16 v[52:55], v[84:87], v[220:223], v[52:55]
	v_mfma_f32_16x16x32_bf16 v[72:75], v[128:131], v[224:227], v[72:75]
	v_mfma_f32_16x16x32_bf16 v[48:51], v[112:115], v[224:227], v[48:51]
	v_mfma_f32_16x16x32_bf16 v[76:79], v[96:99], v[224:227], v[76:79]
	v_mfma_f32_16x16x32_bf16 v[52:55], v[80:83], v[224:227], v[52:55]
	v_add_u32_e32 v141, v47, v38
	v_add_u32_e32 v183, v47, v39
	v_add_u32_e32 v47, v47, v40
	ds_read_b128 v[80:83], v47 offset:34880
	ds_read_b128 v[84:87], v47 offset:34816
	ds_read_b128 v[88:91], v141 offset:48704
	ds_read_b128 v[92:95], v141 offset:48640
	ds_read_b128 v[96:99], v141 offset:46400
	ds_read_b128 v[100:103], v141 offset:46336
	ds_read_b128 v[104:107], v141 offset:44096
	ds_read_b128 v[108:111], v141 offset:44032
	ds_read_b128 v[112:115], v183 offset:34880
	ds_read_b128 v[116:119], v183 offset:34816
	ds_read_b128 v[120:123], v141 offset:39488
	ds_read_b128 v[124:127], v141 offset:39424
	ds_read_b128 v[128:131], v141 offset:37184
	ds_read_b128 v[132:135], v141 offset:37120
	ds_read_b128 v[136:139], v141 offset:34880
	ds_read_b128 v[142:145], v141 offset:34816
	s_waitcnt lgkmcnt(15)
; #define LAS __attribute__((address_space(3)))
; #define SC_BAR() do { asm volatile("s_waitcnt lgkmcnt(0)" ::: "memory"); __builtin_amdgcn_s_barrier(); asm volatile("" ::: "memory"); } while (0)
; #define PIN8(a) asm volatile("" : "+v"(a[0]), "+v"(a[1]), "+v"(a[2]), "+v"(a[3]), "+v"(a[4]), "+v"(a[5]), "+v"(a[6]), "+v"(a[7]))
; #define PIN16(a) asm volatile("" : "+v"(a[0]), "+v"(a[1]), "+v"(a[2]), "+v"(a[3]), "+v"(a[4]), "+v"(a[5]), "+v"(a[6]), "+v"(a[7]), "+v"(a[8]), "+v"(a[9]), "+v"(a[10]), "+v"(a[11]), "+v"(a[12]), "+v"(a[13]), "+v"(a[14]), "+v"(a[15]))
; __device__ __forceinline__ void gdn_scan(const Params& P, LAS unsigned char* lds, int sb, int tid, int lane, int wave) {
;     ...
;             for (int rho = 0; rho < 4; ++rho) Oc[rho] = __builtin_amdgcn_mfma_f32_16x16x32_bf16(fB[rho * 4 + s], Bs[s], Oc[rho], 0, 0, 0);
;         __builtin_amdgcn_sched_barrier(0);
; #pragma unroll
;         for (int rho = 0; rho < 4; ++rho)
; #pragma unroll
;             for (int s = 0; s < 2; ++s) fD[rho * 2 + s] = *(const LAS bf16x8*)(buf + SC_ATT + (16 * rho + col) * 144 + (32 * s + 8 * g) * 2);
;         bf16x8 Bv[2];
;         Bv[0] = pack_b(Vn[0], Vn[1]); Bv[1] = pack_b(Vn[2], Vn[3]);
; #pragma unroll
;         for (int tau = 0; tau < 8; ++tau) S[tau] = S[tau] * dec;
;         __builtin_amdgcn_sched_barrier(0);
;         PIN16(fC);
; #pragma unroll
;         for (int s = 0; s < 2; ++s)
; #pragma unroll
;             for (int tau = 0; tau < 8; ++tau) S[tau] = __builtin_amdgcn_mfma_f32_16x16x32_bf16(fC[tau * 2 + s], Bv[s], S[tau], 0, 0, 0);
;         __builtin_amdgcn_sched_barrier(0);
;         PIN8(fD);
; #pragma unroll
;         for (int s = 0; s < 2; ++s)
; #pragma unroll
;             for (int rho = 0; rho < 4; ++rho) Oc[rho] = __builtin_amdgcn_mfma_f32_16x16x32_bf16(fD[rho * 2 + s], Bv[s], Oc[rho], 0, 0, 0);
;         LAS float* ot = (LAS float*)(lds + SC_OT + par * (64 * 36 * 4)) + 16 * wave + col;
; #pragma unroll
;         for (int rho = 0; rho < 4; ++rho)
; #pragma unroll
;             for (int i = 0; i < 4; ++i) ot[(16 * rho + 4 * g + i) * 36] = Oc[rho][i];
;         SC_BAR();
	v_mfma_f32_16x16x32_bf16 v[208:211], v[208:211], v[212:215], 0
	v_pk_mul_f32 v[32:33], v[34:35], v[32:33] op_sel_hi:[0,1]
	v_mfma_f32_16x16x32_bf16 v[192:195], v[192:195], v[212:215], 0
	v_pk_mul_f32 v[30:31], v[34:35], v[30:31] op_sel_hi:[0,1]
	v_mfma_f32_16x16x32_bf16 v[174:177], v[174:177], v[212:215], 0
	v_pk_mul_f32 v[28:29], v[34:35], v[28:29] op_sel_hi:[0,1]
	v_mfma_f32_16x16x32_bf16 v[56:59], v[158:161], v[212:215], 0
	v_pk_mul_f32 v[26:27], v[34:35], v[26:27] op_sel_hi:[0,1]
	v_mfma_f32_16x16x32_bf16 v[158:161], v[204:207], v[216:219], v[208:211]
	v_pk_mul_f32 v[24:25], v[34:35], v[24:25] op_sel_hi:[0,1]
	v_mfma_f32_16x16x32_bf16 v[188:191], v[188:191], v[216:219], v[192:195]
	v_pk_mul_f32 v[22:23], v[34:35], v[22:23] op_sel_hi:[0,1]
	v_mfma_f32_16x16x32_bf16 v[170:173], v[170:173], v[216:219], v[174:177]
	v_pk_mul_f32 v[20:21], v[34:35], v[20:21] op_sel_hi:[0,1]
	v_mfma_f32_16x16x32_bf16 v[56:59], v[154:157], v[216:219], v[56:59]
	v_pk_mul_f32 v[18:19], v[34:35], v[18:19] op_sel_hi:[0,1]
	v_mfma_f32_16x16x32_bf16 v[60:63], v[200:203], v[220:223], v[158:161]
	v_pk_mul_f32 v[16:17], v[34:35], v[16:17] op_sel_hi:[0,1]
	v_cvt_pk_bf16_f32 v68, v72, v73
	v_mfma_f32_16x16x32_bf16 v[154:157], v[184:187], v[220:223], v[188:191]
	v_pk_mul_f32 v[14:15], v[34:35], v[14:15] op_sel_hi:[0,1]
	v_cvt_pk_bf16_f32 v69, v74, v75
	v_mfma_f32_16x16x32_bf16 v[158:161], v[166:169], v[220:223], v[170:173]
	v_pk_mul_f32 v[12:13], v[34:35], v[12:13] op_sel_hi:[0,1]
	v_cvt_pk_bf16_f32 v70, v48, v49
	v_mfma_f32_16x16x32_bf16 v[56:59], v[150:153], v[220:223], v[56:59]
	v_pk_mul_f32 v[10:11], v[34:35], v[10:11] op_sel_hi:[0,1]
	v_cvt_pk_bf16_f32 v71, v50, v51
	v_mfma_f32_16x16x32_bf16 v[60:63], v[196:199], v[224:227], v[60:63]
	v_pk_mul_f32 v[8:9], v[34:35], v[8:9] op_sel_hi:[0,1]
	v_cvt_pk_bf16_f32 v48, v76, v77
	v_mfma_f32_16x16x32_bf16 v[64:67], v[178:181], v[224:227], v[154:157]
	v_pk_mul_f32 v[6:7], v[34:35], v[6:7] op_sel_hi:[0,1]
	v_cvt_pk_bf16_f32 v49, v78, v79
	v_mfma_f32_16x16x32_bf16 v[150:153], v[162:165], v[224:227], v[158:161]
	v_pk_mul_f32 v[4:5], v[34:35], v[4:5] op_sel_hi:[0,1]
	v_cvt_pk_bf16_f32 v50, v52, v53
	v_mfma_f32_16x16x32_bf16 v[56:59], v[146:149], v[224:227], v[56:59]
	v_pk_mul_f32 v[2:3], v[34:35], v[2:3] op_sel_hi:[0,1]
	v_cvt_pk_bf16_f32 v51, v54, v55
	ds_read_b128 v[52:55], v183 offset:53312
	ds_read_b128 v[72:75], v183 offset:53248
	ds_read_b128 v[76:79], v141 offset:57920
	ds_read_b128 v[146:149], v141 offset:57856
	ds_read_b128 v[154:157], v141 offset:55616
	ds_read_b128 v[158:161], v141 offset:55552
	ds_read_b128 v[162:165], v141 offset:53312
	ds_read_b128 v[166:169], v141 offset:53248
	s_waitcnt lgkmcnt(8)
	s_nop 0
	v_mfma_f32_16x16x32_bf16 v[30:33], v[142:145], v[68:71], v[30:33]
	v_mfma_f32_16x16x32_bf16 v[26:29], v[132:135], v[68:71], v[26:29]
	v_mfma_f32_16x16x32_bf16 v[22:25], v[124:127], v[68:71], v[22:25]
	v_mfma_f32_16x16x32_bf16 v[18:21], v[116:119], v[68:71], v[18:21]
	v_mfma_f32_16x16x32_bf16 v[14:17], v[108:111], v[68:71], v[14:17]
	v_mfma_f32_16x16x32_bf16 v[10:13], v[100:103], v[68:71], v[10:13]
	v_mfma_f32_16x16x32_bf16 v[6:9], v[92:95], v[68:71], v[6:9]
	v_mfma_f32_16x16x32_bf16 v[2:5], v[84:87], v[68:71], v[2:5]
	v_mfma_f32_16x16x32_bf16 v[30:33], v[136:139], v[48:51], v[30:33]
	v_mfma_f32_16x16x32_bf16 v[26:29], v[128:131], v[48:51], v[26:29]
	v_mfma_f32_16x16x32_bf16 v[22:25], v[120:123], v[48:51], v[22:25]
	v_mfma_f32_16x16x32_bf16 v[18:21], v[112:115], v[48:51], v[18:21]
	v_mfma_f32_16x16x32_bf16 v[14:17], v[104:107], v[48:51], v[14:17]
	v_mfma_f32_16x16x32_bf16 v[10:13], v[96:99], v[48:51], v[10:13]
	v_mfma_f32_16x16x32_bf16 v[6:9], v[88:91], v[48:51], v[6:9]
	v_mfma_f32_16x16x32_bf16 v[2:5], v[80:83], v[48:51], v[2:5]
	s_waitcnt lgkmcnt(0)
	s_mulk_i32 s6, 0x2400
	v_mfma_f32_16x16x32_bf16 v[60:63], v[166:169], v[68:71], v[60:63]
	v_add_u32_e32 v34, s6, v35
	v_add_u32_e32 v47, v34, v41
	s_add_i32 s1, s1, 1
	v_mfma_f32_16x16x32_bf16 v[64:67], v[158:161], v[68:71], v[64:67]
	s_add_i32 s3, s3, 4
	s_cmpk_eq_i32 s1, 0x80
	v_mfma_f32_16x16x32_bf16 v[60:63], v[162:165], v[48:51], v[60:63]
	v_cvt_pk_bf16_f32 v212, v30, v31
	v_cvt_pk_bf16_f32 v213, v32, v33
	v_cvt_pk_bf16_f32 v214, v26, v27
	v_cvt_pk_bf16_f32 v215, v28, v29
	v_cvt_pk_bf16_f32 v216, v22, v23
	v_cvt_pk_bf16_f32 v217, v24, v25
	v_cvt_pk_bf16_f32 v218, v18, v19
	v_cvt_pk_bf16_f32 v219, v20, v21
	ds_write2_b32 v47, v60, v61 offset1:36
	ds_write_b32 v47, v62 offset:288
	v_mfma_f32_16x16x32_bf16 v[64:67], v[154:157], v[48:51], v[64:67]
	v_add_u32_e32 v60, v34, v42
	ds_write_b32 v60, v63
	v_add_u32_e32 v60, 0x800, v47
	v_mfma_f32_16x16x32_bf16 v[56:59], v[72:75], v[68:71], v[56:59]
	v_cvt_pk_bf16_f32 v220, v14, v15
	v_cvt_pk_bf16_f32 v221, v16, v17
	v_cvt_pk_bf16_f32 v222, v10, v11
	v_cvt_pk_bf16_f32 v223, v12, v13
	ds_write2_b32 v60, v64, v65 offset0:64 offset1:100
	v_mfma_f32_16x16x32_bf16 v[60:63], v[146:149], v[68:71], v[150:153]
	v_add_u32_e32 v64, v34, v43
	ds_write_b32 v47, v66 offset:2592
	ds_write_b32 v64, v67
	v_mfma_f32_16x16x32_bf16 v[60:63], v[76:79], v[48:51], v[60:63]
	v_add_u32_e32 v64, 0x1000, v47
	v_cvt_pk_bf16_f32 v224, v6, v7
	v_cvt_pk_bf16_f32 v225, v8, v9
	v_cvt_pk_bf16_f32 v226, v2, v3
	v_cvt_pk_bf16_f32 v227, v4, v5
	s_nop 2
	ds_write2_b32 v64, v60, v61 offset0:128 offset1:164
	ds_write_b32 v47, v62 offset:4896
	v_mfma_f32_16x16x32_bf16 v[48:51], v[52:55], v[48:51], v[56:59]
	v_add_u32_e32 v60, v34, v44
	ds_write_b32 v60, v63
	v_add_u32_e32 v60, 0x1800, v47
	v_add_u32_e32 v34, v34, v45
	s_nop 3
	ds_write2_b32 v60, v48, v49 offset0:192 offset1:228
	ds_write_b32 v47, v50 offset:7200
	ds_write_b32 v34, v51
	s_waitcnt lgkmcnt(0)
	s_barrier
	s_cbranch_scc0 .LBB0_2145
	s_branch .LBB0_2153

; #define SC_BAR() do { asm volatile("s_waitcnt lgkmcnt(0)" ::: "memory"); __builtin_amdgcn_s_barrier(); asm volatile("" ::: "memory"); } while (0)
; #define SC_WAITSET(set, cnt) asm volatile("s_waitcnt " cnt : "+v"(rs[set][0]), "+v"(rs[set][1]), "+v"(rs[set][2]), "+v"(rs[set][3]), "+v"(rs[set][4]), "+v"(rs[set][5]), "+v"(rs[set][6]), "+v"(rs[set][7]), \
;             "+v"(rs[set][8]), "+v"(rs[set][9]), "+v"(rs[set][10]), "+v"(rs[set][11]), "+v"(rs[set][12]), "+v"(rs[set][13]), "+v"(rs[set][14]) :: "memory")
; #define SC_NEED(c) do { unsigned sp_ = 0; while (*(volatile LAS unsigned*)(lds + SC_RDY) <= (unsigned)(c) && ++sp_ < (1u << 24)) __builtin_amdgcn_s_sleep(2); } while (0)
; #define SC_INTERVAL(set) do { SC_WAITSET(set, "vmcnt(30)"); SC_WRITE(set, (n2 + 1) & 1); SC_WAITSET(set, "lgkmcnt(0)"); if (n2 + 1 + DEP < 128) SC_NEED(n2 + 1 + DEP); SC_ISSUE(set, item0 + ((n2 + 1 + DEP) & 127)); SC_BAR(); ++n2; } while (0)
; __device__ __forceinline__ void gdn_scan(const Params& P, LAS unsigned char* lds, int sb, int tid, int lane, int wave) {
;     ...
;         SC_NEED(0); SC_ISSUE(0, item0);
;         SC_WAITSET(0, "vmcnt(0)"); SC_WRITE(0, 0); SC_WAITSET(0, "lgkmcnt(0)");
;         SC_NEED(3); SC_ISSUE(1, item0 + 1); SC_ISSUE(2, item0 + 2); SC_ISSUE(0, item0 + 3);
;         SC_BAR();
;         int n2 = 0;
;     ...
; #pragma unroll 1
;         for (int it = 0; it < NCH / 3; ++it) { SC_INTERVAL(1); SC_INTERVAL(2); SC_INTERVAL(0); }
.LBB0_2168:
	s_and_b32 s6, s34, 0x7f
	s_or_b32 s6, s6, s3
	s_lshl_b32 s7, s6, 14
	s_add_u32 s30, s24, s7
	s_addc_u32 s54, s25, 0
	s_lshl_b32 s6, s6, 13
	s_add_u32 s6, s27, s6
	s_addc_u32 s7, s33, 0
	s_add_u32 s22, s30, 0x9c00000
	s_addc_u32 s23, s54, 0
	s_add_u32 s34, s30, 0x9c01000
	s_addc_u32 s35, s54, 0
	s_add_u32 s38, s30, 0x9c02000
	s_addc_u32 s39, s54, 0
	s_add_u32 s52, s30, 0x9c03000
	s_addc_u32 s53, s54, 0
	s_add_u32 s72, s30, 0xbc00000
	s_addc_u32 s73, s54, 0
	s_add_u32 s74, s30, 0xbc01000
	s_addc_u32 s75, s54, 0
	s_add_u32 s94, s30, 0xbc02000
	s_addc_u32 s95, s54, 0
	s_add_u32 s96, s30, 0xbc03000
	s_addc_u32 s97, s54, 0
	s_nop 4
	ds_write_b128 v189, v[34:37]
	ds_write_b128 v189, v[38:41] offset:4352
	global_load_dwordx4 v[34:37], v1, s[22:23] sc0 sc1
	ds_write_b128 v189, v[42:45] offset:8704
	global_load_dwordx4 v[38:41], v1, s[34:35] sc0 sc1
	ds_write_b128 v189, v[46:49] offset:13056
	global_load_dwordx4 v[42:45], v1, s[38:39] sc0 sc1
	ds_write_b128 v189, v[50:53] offset:17408
	global_load_dwordx4 v[46:49], v1, s[52:53] sc0 sc1
	ds_write_b128 v189, v[54:57] offset:21760
	global_load_dwordx4 v[50:53], v1, s[72:73] sc0 sc1
	ds_write_b128 v189, v[58:61] offset:26112
	global_load_dwordx4 v[54:57], v1, s[74:75] sc0 sc1
	ds_write_b128 v189, v[62:65] offset:30464
	global_load_dwordx4 v[58:61], v1, s[94:95] sc0 sc1
	ds_write_b128 v190, v[126:129] offset:34816
	global_load_dwordx4 v[62:65], v1, s[96:97] sc0 sc1
	s_add_u32 s22, s30, 0xcc00000
	s_addc_u32 s23, s54, 0
	s_add_u32 s34, s30, 0xcc01000
	s_addc_u32 s35, s54, 0
	s_add_u32 s38, s30, 0xcc02000
	s_addc_u32 s39, s54, 0
	s_add_u32 s52, s30, 0xcc03000
	s_addc_u32 s53, s54, 0
	s_add_u32 s72, s6, 0x1000
	s_addc_u32 s73, s7, 0
	s_add_u32 s30, s30, s0
	s_addc_u32 s54, s54, s1
	s_add_u32 s74, s30, 0xac00000
	s_addc_u32 s75, s54, 0
	s_nop 4
	ds_write_b128 v190, v[130:133] offset:39424
	global_load_dwordx4 v[126:129], v1, s[22:23] sc0 sc1
	ds_write_b128 v190, v[134:137] offset:44032
	global_load_dwordx4 v[130:133], v1, s[34:35] sc0 sc1
	ds_write_b128 v190, v[138:141] offset:48640
	global_load_dwordx4 v[134:137], v1, s[38:39] sc0 sc1
	ds_write_b128 v190, v[142:145] offset:53248
	global_load_dwordx4 v[138:141], v1, s[52:53] sc0 sc1
	ds_write_b128 v190, v[146:149] offset:57856
	global_load_dwordx4 v[142:145], v1, s[6:7] sc0 sc1
	ds_write_b128 v201, v[150:153]
	global_load_dwordx4 v[146:149], v1, s[72:73] sc0 sc1
	global_load_dwordx4 v[150:153], v1, s[74:75] sc0 sc1
	s_waitcnt lgkmcnt(0)
	s_barrier
	s_add_i32 s29, s29, 1
	s_cmp_eq_u32 s29, 42
	s_cbranch_scc1 .LBB0_2204
.LBB0_2169:
	s_mov_b32 s30, s31
	s_and_b32 s31, s31, 1
	s_waitcnt vmcnt(30)
	s_xor_b32 s6, s31, 1
	s_mul_i32 s7, s6, 0xf400
	s_add_i32 s7, s7, 0
	v_add_u32_e32 v189, s7, v186
	v_add_u32_e32 v190, s7, v187
	v_lshl_add_u32 v201, s6, 12, v183
	s_add_i32 s34, s30, 4
	v_mov_b32_e32 v200, s28
	ds_read_b32 v200, v200
	s_waitcnt lgkmcnt(0)
	v_cmp_lt_u32_e32 vcc, s34, v200
	s_cbranch_vccnz .LBB0_2180
	s_mov_b32 s35, 0xfffff8
	s_branch .LBB0_2172

; #define SC_BAR() do { asm volatile("s_waitcnt lgkmcnt(0)" ::: "memory"); __builtin_amdgcn_s_barrier(); asm volatile("" ::: "memory"); } while (0)
; #define SC_WAITSET(set, cnt) asm volatile("s_waitcnt " cnt : "+v"(rs[set][0]), "+v"(rs[set][1]), "+v"(rs[set][2]), "+v"(rs[set][3]), "+v"(rs[set][4]), "+v"(rs[set][5]), "+v"(rs[set][6]), "+v"(rs[set][7]), \
;             "+v"(rs[set][8]), "+v"(rs[set][9]), "+v"(rs[set][10]), "+v"(rs[set][11]), "+v"(rs[set][12]), "+v"(rs[set][13]), "+v"(rs[set][14]) :: "memory")
; #define SC_NEED(c) do { unsigned sp_ = 0; while (*(volatile LAS unsigned*)(lds + SC_RDY) <= (unsigned)(c) && ++sp_ < (1u << 24)) __builtin_amdgcn_s_sleep(2); } while (0)
; #define SC_INTERVAL(set) do { SC_WAITSET(set, "vmcnt(30)"); SC_WRITE(set, (n2 + 1) & 1); SC_WAITSET(set, "lgkmcnt(0)"); if (n2 + 1 + DEP < 128) SC_NEED(n2 + 1 + DEP); SC_ISSUE(set, item0 + ((n2 + 1 + DEP) & 127)); SC_BAR(); ++n2; } while (0)
; __device__ __forceinline__ void gdn_scan(const Params& P, LAS unsigned char* lds, int sb, int tid, int lane, int wave) {
;     ...
;         SC_NEED(0); SC_ISSUE(0, item0);
;         SC_WAITSET(0, "vmcnt(0)"); SC_WRITE(0, 0); SC_WAITSET(0, "lgkmcnt(0)");
;         SC_NEED(3); SC_ISSUE(1, item0 + 1); SC_ISSUE(2, item0 + 2); SC_ISSUE(0, item0 + 3);
;         SC_BAR();
;         int n2 = 0;
;     ...
; #pragma unroll 1
;         for (int it = 0; it < NCH / 3; ++it) { SC_INTERVAL(1); SC_INTERVAL(2); SC_INTERVAL(0); }
.LBB0_2172:
	v_mov_b32_e32 v200, s28
	s_sleep 2
	ds_read_b32 v200, v200
	s_mov_b64 s[22:23], -1
	s_waitcnt lgkmcnt(0)
	v_cmp_lt_u32_e32 vcc, s34, v200
	s_cbranch_vccnz .LBB0_2171
	v_mov_b32_e32 v200, s28
	s_sleep 2
	ds_read_b32 v200, v200
	s_waitcnt lgkmcnt(0)
	v_cmp_ge_u32_e32 vcc, s34, v200
	s_cbranch_vccz .LBB0_2171
	v_mov_b32_e32 v200, s28
	s_sleep 2
	ds_read_b32 v200, v200
	s_waitcnt lgkmcnt(0)
	v_cmp_ge_u32_e32 vcc, s34, v200
	s_cbranch_vccz .LBB0_2171
	v_mov_b32_e32 v200, s28
	s_sleep 2
	ds_read_b32 v200, v200
	s_waitcnt lgkmcnt(0)
	v_cmp_ge_u32_e32 vcc, s34, v200
	s_cbranch_vccz .LBB0_2171
	v_mov_b32_e32 v200, s28
	s_sleep 2
	ds_read_b32 v200, v200
	s_waitcnt lgkmcnt(0)
	v_cmp_ge_u32_e32 vcc, s34, v200
	s_cbranch_vccz .LBB0_2171
	v_mov_b32_e32 v200, s28
	s_sleep 2
	ds_read_b32 v200, v200
	s_waitcnt lgkmcnt(0)
	v_cmp_ge_u32_e32 vcc, s34, v200
	s_cbranch_vccz .LBB0_2171
	v_mov_b32_e32 v200, s28
	s_sleep 2
	ds_read_b32 v200, v200
	s_cmp_eq_u32 s35, 0
	s_cselect_b64 s[22:23], -1, 0
	s_waitcnt lgkmcnt(0)
	v_cmp_lt_u32_e32 vcc, s34, v200
	s_or_b64 s[22:23], vcc, s[22:23]
	s_andn2_b64 vcc, exec, s[22:23]
	s_mov_b64 s[22:23], -1
	s_cbranch_vccz .LBB0_2171
	v_mov_b32_e32 v200, s28
	s_sleep 2
	ds_read_b32 v200, v200
	s_add_i32 s35, s35, -8
	s_waitcnt lgkmcnt(0)
	v_cmp_lt_u32_e64 s[22:23], s34, v200
	s_branch .LBB0_2171
.LBB0_2180:
	s_or_b32 s54, s34, s3
	s_lshl_b64 s[22:23], s[54:55], 14
	s_add_u32 vcc_lo, s24, s22
	s_addc_u32 vcc_hi, s25, s23
	s_lshl_b64 s[22:23], s[54:55], 13
	s_add_u32 s22, s27, s22
	s_addc_u32 s23, s33, s23
	s_add_u32 s34, vcc_lo, 0x9c00000
	s_addc_u32 s35, vcc_hi, 0
	s_add_u32 s38, vcc_lo, 0x9c01000
	s_addc_u32 s39, vcc_hi, 0
	s_add_u32 s52, vcc_lo, 0x9c02000
	s_addc_u32 s53, vcc_hi, 0
	s_add_u32 s72, vcc_lo, 0x9c03000
	s_addc_u32 s73, vcc_hi, 0
	s_add_u32 s74, vcc_lo, 0xbc00000
	s_addc_u32 s75, vcc_hi, 0
	s_add_u32 s94, vcc_lo, 0xbc01000
	s_addc_u32 s95, vcc_hi, 0
	s_add_u32 s96, vcc_lo, 0xbc02000
	s_addc_u32 s97, vcc_hi, 0
	s_add_u32 s6, vcc_lo, 0xbc03000
	s_addc_u32 s7, vcc_hi, 0
	s_nop 4
	ds_write_b128 v189, v[66:69]
	ds_write_b128 v189, v[70:73] offset:4352
	global_load_dwordx4 v[66:69], v1, s[34:35] sc0 sc1
	ds_write_b128 v189, v[74:77] offset:8704
	global_load_dwordx4 v[70:73], v1, s[38:39] sc0 sc1
	ds_write_b128 v189, v[78:81] offset:13056
	global_load_dwordx4 v[74:77], v1, s[52:53] sc0 sc1
	ds_write_b128 v189, v[82:85] offset:17408
	global_load_dwordx4 v[78:81], v1, s[72:73] sc0 sc1
	ds_write_b128 v189, v[86:89] offset:21760
	global_load_dwordx4 v[82:85], v1, s[74:75] sc0 sc1
	ds_write_b128 v189, v[90:93] offset:26112
	global_load_dwordx4 v[86:89], v1, s[94:95] sc0 sc1
	ds_write_b128 v189, v[94:97] offset:30464
	global_load_dwordx4 v[90:93], v1, s[96:97] sc0 sc1
	ds_write_b128 v190, v[154:157] offset:34816
	global_load_dwordx4 v[94:97], v1, s[6:7] sc0 sc1
	s_add_u32 s6, vcc_lo, 0xcc00000
	s_addc_u32 s7, vcc_hi, 0
	s_add_u32 s34, vcc_lo, 0xcc01000
	s_addc_u32 s35, vcc_hi, 0
	s_add_u32 s38, vcc_lo, 0xcc02000
	s_addc_u32 s39, vcc_hi, 0
	s_add_u32 s52, vcc_lo, 0xcc03000
	s_addc_u32 s53, vcc_hi, 0
	s_add_u32 s72, s22, 0x1000
	s_addc_u32 s73, s23, 0
	s_add_u32 s54, vcc_lo, s0
	s_addc_u32 s75, vcc_hi, s1
	s_add_u32 s74, s54, 0xac00000
	s_addc_u32 s75, s75, 0
	s_nop 4
	ds_write_b128 v190, v[158:161] offset:39424
	global_load_dwordx4 v[154:157], v1, s[6:7] sc0 sc1
	ds_write_b128 v190, v[162:165] offset:44032
	global_load_dwordx4 v[158:161], v1, s[34:35] sc0 sc1
	ds_write_b128 v190, v[166:169] offset:48640
	global_load_dwordx4 v[162:165], v1, s[38:39] sc0 sc1
	ds_write_b128 v190, v[170:173] offset:53248
	global_load_dwordx4 v[166:169], v1, s[52:53] sc0 sc1
	ds_write_b128 v190, v[174:177] offset:57856
	global_load_dwordx4 v[170:173], v1, s[22:23] sc0 sc1
	ds_write_b128 v201, v[178:181]
	global_load_dwordx4 v[174:177], v1, s[72:73] sc0 sc1
	global_load_dwordx4 v[178:181], v1, s[74:75] sc0 sc1
	s_waitcnt lgkmcnt(0)
	s_barrier
	s_waitcnt vmcnt(30)
	s_mul_i32 s6, s31, 0xf400
	s_add_i32 s6, s6, 0
	v_add_u32_e32 v189, s6, v186
	v_add_u32_e32 v190, s6, v187
	v_lshl_add_u32 v201, s31, 12, v183
	s_add_i32 s31, s30, 5
	s_cmpk_gt_u32 s30, 0x7a
	s_cbranch_scc1 .LBB0_2192
	v_mov_b32_e32 v200, s28
	ds_read_b32 v200, v200
	s_waitcnt lgkmcnt(0)
	v_cmp_lt_u32_e32 vcc, s31, v200
	s_cbranch_vccnz .LBB0_2192
	s_mov_b32 s34, 0xfffff8
	s_branch .LBB0_2184

; #define SC_BAR() do { asm volatile("s_waitcnt lgkmcnt(0)" ::: "memory"); __builtin_amdgcn_s_barrier(); asm volatile("" ::: "memory"); } while (0)
; #define SC_WAITSET(set, cnt) asm volatile("s_waitcnt " cnt : "+v"(rs[set][0]), "+v"(rs[set][1]), "+v"(rs[set][2]), "+v"(rs[set][3]), "+v"(rs[set][4]), "+v"(rs[set][5]), "+v"(rs[set][6]), "+v"(rs[set][7]), \
;             "+v"(rs[set][8]), "+v"(rs[set][9]), "+v"(rs[set][10]), "+v"(rs[set][11]), "+v"(rs[set][12]), "+v"(rs[set][13]), "+v"(rs[set][14]) :: "memory")
; #define SC_NEED(c) do { unsigned sp_ = 0; while (*(volatile LAS unsigned*)(lds + SC_RDY) <= (unsigned)(c) && ++sp_ < (1u << 24)) __builtin_amdgcn_s_sleep(2); } while (0)
; #define SC_INTERVAL(set) do { SC_WAITSET(set, "vmcnt(30)"); SC_WRITE(set, (n2 + 1) & 1); SC_WAITSET(set, "lgkmcnt(0)"); if (n2 + 1 + DEP < 128) SC_NEED(n2 + 1 + DEP); SC_ISSUE(set, item0 + ((n2 + 1 + DEP) & 127)); SC_BAR(); ++n2; } while (0)
; __device__ __forceinline__ void gdn_scan(const Params& P, LAS unsigned char* lds, int sb, int tid, int lane, int wave) {
;     ...
;         SC_NEED(0); SC_ISSUE(0, item0);
;         SC_WAITSET(0, "vmcnt(0)"); SC_WRITE(0, 0); SC_WAITSET(0, "lgkmcnt(0)");
;         SC_NEED(3); SC_ISSUE(1, item0 + 1); SC_ISSUE(2, item0 + 2); SC_ISSUE(0, item0 + 3);
;         SC_BAR();
;         int n2 = 0;
;     ...
; #pragma unroll 1
;         for (int it = 0; it < NCH / 3; ++it) { SC_INTERVAL(1); SC_INTERVAL(2); SC_INTERVAL(0); }
.LBB0_2184:
	v_mov_b32_e32 v200, s28
	s_sleep 2
	ds_read_b32 v200, v200
	s_mov_b64 s[22:23], -1
	s_waitcnt lgkmcnt(0)
	v_cmp_lt_u32_e32 vcc, s31, v200
	s_cbranch_vccnz .LBB0_2183
	v_mov_b32_e32 v200, s28
	s_sleep 2
	ds_read_b32 v200, v200
	s_waitcnt lgkmcnt(0)
	v_cmp_ge_u32_e32 vcc, s31, v200
	s_cbranch_vccz .LBB0_2183
	v_mov_b32_e32 v200, s28
	s_sleep 2
	ds_read_b32 v200, v200
	s_waitcnt lgkmcnt(0)
	v_cmp_ge_u32_e32 vcc, s31, v200
	s_cbranch_vccz .LBB0_2183
	v_mov_b32_e32 v200, s28
	s_sleep 2
	ds_read_b32 v200, v200
	s_waitcnt lgkmcnt(0)
	v_cmp_ge_u32_e32 vcc, s31, v200
	s_cbranch_vccz .LBB0_2183
	v_mov_b32_e32 v200, s28
	s_sleep 2
	ds_read_b32 v200, v200
	s_waitcnt lgkmcnt(0)
	v_cmp_ge_u32_e32 vcc, s31, v200
	s_cbranch_vccz .LBB0_2183
	v_mov_b32_e32 v200, s28
	s_sleep 2
	ds_read_b32 v200, v200
	s_waitcnt lgkmcnt(0)
	v_cmp_ge_u32_e32 vcc, s31, v200
	s_cbranch_vccz .LBB0_2183
	v_mov_b32_e32 v200, s28
	s_sleep 2
	ds_read_b32 v200, v200
	s_cmp_eq_u32 s34, 0
	s_cselect_b64 s[6:7], -1, 0
	s_waitcnt lgkmcnt(0)
	v_cmp_lt_u32_e32 vcc, s31, v200
	s_or_b64 s[6:7], vcc, s[6:7]
	s_andn2_b64 vcc, exec, s[6:7]
	s_cbranch_vccz .LBB0_2183
	v_mov_b32_e32 v200, s28
	s_sleep 2
	ds_read_b32 v200, v200
	s_add_i32 s34, s34, -8
	s_waitcnt lgkmcnt(0)
	v_cmp_lt_u32_e64 s[22:23], s31, v200
	s_branch .LBB0_2183
.LBB0_2192:
	s_and_b32 s6, s31, 0x7f
	s_or_b32 s6, s6, s3
	s_lshl_b32 s7, s6, 14
	s_add_u32 s31, s24, s7
	s_addc_u32 s54, s25, 0
	s_lshl_b32 s6, s6, 13
	s_add_u32 s6, s27, s6
	s_addc_u32 s7, s33, 0
	s_add_u32 s22, s31, 0x9c00000
	s_addc_u32 s23, s54, 0
	s_add_u32 s34, s31, 0x9c01000
	s_addc_u32 s35, s54, 0
	s_add_u32 s38, s31, 0x9c02000
	s_addc_u32 s39, s54, 0
	s_add_u32 s52, s31, 0x9c03000
	s_addc_u32 s53, s54, 0
	s_add_u32 s72, s31, 0xbc00000
	s_addc_u32 s73, s54, 0
	s_add_u32 s74, s31, 0xbc01000
	s_addc_u32 s75, s54, 0
	s_add_u32 s94, s31, 0xbc02000
	s_addc_u32 s95, s54, 0
	s_add_u32 s96, s31, 0xbc03000
	s_addc_u32 s97, s54, 0
	s_nop 4
	ds_write_b128 v189, v[2:5]
	ds_write_b128 v189, v[6:9] offset:4352
	global_load_dwordx4 v[2:5], v1, s[22:23] sc0 sc1
	ds_write_b128 v189, v[10:13] offset:8704
	global_load_dwordx4 v[6:9], v1, s[34:35] sc0 sc1
	ds_write_b128 v189, v[14:17] offset:13056
	global_load_dwordx4 v[10:13], v1, s[38:39] sc0 sc1
	ds_write_b128 v189, v[18:21] offset:17408
	global_load_dwordx4 v[14:17], v1, s[52:53] sc0 sc1
	ds_write_b128 v189, v[22:25] offset:21760
	global_load_dwordx4 v[18:21], v1, s[72:73] sc0 sc1
	ds_write_b128 v189, v[26:29] offset:26112
	global_load_dwordx4 v[22:25], v1, s[74:75] sc0 sc1
	ds_write_b128 v189, v[30:33] offset:30464
	global_load_dwordx4 v[26:29], v1, s[94:95] sc0 sc1
	ds_write_b128 v190, v[98:101] offset:34816
	global_load_dwordx4 v[30:33], v1, s[96:97] sc0 sc1
	s_add_u32 s22, s31, 0xcc00000
	s_addc_u32 s23, s54, 0
	s_add_u32 s34, s31, 0xcc01000
	s_addc_u32 s35, s54, 0
	s_add_u32 s38, s31, 0xcc02000
	s_addc_u32 s39, s54, 0
	s_add_u32 s52, s31, 0xcc03000
	s_addc_u32 s53, s54, 0
	s_add_u32 s72, s6, 0x1000
	s_addc_u32 s73, s7, 0
	s_add_u32 s31, s31, s0
	s_addc_u32 s54, s54, s1
	s_add_u32 s74, s31, 0xac00000
	s_addc_u32 s75, s54, 0
	s_nop 4
	ds_write_b128 v190, v[102:105] offset:39424
	global_load_dwordx4 v[98:101], v1, s[22:23] sc0 sc1
	ds_write_b128 v190, v[106:109] offset:44032
	global_load_dwordx4 v[102:105], v1, s[34:35] sc0 sc1
	ds_write_b128 v190, v[110:113] offset:48640
	global_load_dwordx4 v[106:109], v1, s[38:39] sc0 sc1
	ds_write_b128 v190, v[114:117] offset:53248
	global_load_dwordx4 v[110:113], v1, s[52:53] sc0 sc1
	ds_write_b128 v190, v[118:121] offset:57856
	global_load_dwordx4 v[114:117], v1, s[6:7] sc0 sc1
	ds_write_b128 v201, v[122:125]
	global_load_dwordx4 v[118:121], v1, s[72:73] sc0 sc1
	global_load_dwordx4 v[122:125], v1, s[74:75] sc0 sc1
	s_waitcnt lgkmcnt(0)
	s_barrier
	s_add_i32 s31, s30, 3
	s_waitcnt vmcnt(30)
	s_and_b32 s6, s31, 1
	s_mul_i32 s7, s6, 0xf400
	s_add_i32 s7, s7, 0
	v_add_u32_e32 v189, s7, v186
	v_add_u32_e32 v190, s7, v187
	v_lshl_add_u32 v201, s6, 12, v183
	s_add_i32 s34, s30, 6
	s_cmpk_gt_u32 s30, 0x79
	s_cbranch_scc1 .LBB0_2168
	v_mov_b32_e32 v200, s28
	ds_read_b32 v200, v200
	s_waitcnt lgkmcnt(0)
	v_cmp_lt_u32_e32 vcc, s34, v200
	s_cbranch_vccnz .LBB0_2168
	s_mov_b32 s30, 0xfffff8
	s_branch .LBB0_2196

; #define SC_BAR() do { asm volatile("s_waitcnt lgkmcnt(0)" ::: "memory"); __builtin_amdgcn_s_barrier(); asm volatile("" ::: "memory"); } while (0)
; #define SC_WAITSET(set, cnt) asm volatile("s_waitcnt " cnt : "+v"(rs[set][0]), "+v"(rs[set][1]), "+v"(rs[set][2]), "+v"(rs[set][3]), "+v"(rs[set][4]), "+v"(rs[set][5]), "+v"(rs[set][6]), "+v"(rs[set][7]), \
;             "+v"(rs[set][8]), "+v"(rs[set][9]), "+v"(rs[set][10]), "+v"(rs[set][11]), "+v"(rs[set][12]), "+v"(rs[set][13]), "+v"(rs[set][14]) :: "memory")
; #define SC_NEED(c) do { unsigned sp_ = 0; while (*(volatile LAS unsigned*)(lds + SC_RDY) <= (unsigned)(c) && ++sp_ < (1u << 24)) __builtin_amdgcn_s_sleep(2); } while (0)
; __device__ __forceinline__ void gdn_scan(const Params& P, LAS unsigned char* lds, int sb, int tid, int lane, int wave) {
;     ...
;         SC_NEED(0); SC_ISSUE(0, item0);
;         SC_WAITSET(0, "vmcnt(0)"); SC_WRITE(0, 0); SC_WAITSET(0, "lgkmcnt(0)");
;         SC_NEED(3); SC_ISSUE(1, item0 + 1); SC_ISSUE(2, item0 + 2); SC_ISSUE(0, item0 + 3);
;         SC_BAR();
;         int n2 = 0;
.LBB0_2196:
	v_mov_b32_e32 v200, s28
	s_sleep 2
	ds_read_b32 v200, v200
	s_mov_b64 s[22:23], -1
	s_waitcnt lgkmcnt(0)
	v_cmp_lt_u32_e32 vcc, s34, v200
	s_cbranch_vccnz .LBB0_2195
	v_mov_b32_e32 v200, s28
	s_sleep 2
	ds_read_b32 v200, v200
	s_waitcnt lgkmcnt(0)
	v_cmp_ge_u32_e32 vcc, s34, v200
	s_cbranch_vccz .LBB0_2195
	v_mov_b32_e32 v200, s28
	s_sleep 2
	ds_read_b32 v200, v200
	s_waitcnt lgkmcnt(0)
	v_cmp_ge_u32_e32 vcc, s34, v200
	s_cbranch_vccz .LBB0_2195
	v_mov_b32_e32 v200, s28
	s_sleep 2
	ds_read_b32 v200, v200
	s_waitcnt lgkmcnt(0)
	v_cmp_ge_u32_e32 vcc, s34, v200
	s_cbranch_vccz .LBB0_2195
	v_mov_b32_e32 v200, s28
	s_sleep 2
	ds_read_b32 v200, v200
	s_waitcnt lgkmcnt(0)
	v_cmp_ge_u32_e32 vcc, s34, v200
	s_cbranch_vccz .LBB0_2195
	v_mov_b32_e32 v200, s28
	s_sleep 2
	ds_read_b32 v200, v200
	s_waitcnt lgkmcnt(0)
	v_cmp_ge_u32_e32 vcc, s34, v200
	s_cbranch_vccz .LBB0_2195
	v_mov_b32_e32 v200, s28
	s_sleep 2
	ds_read_b32 v200, v200
	s_cmp_eq_u32 s30, 0
	s_cselect_b64 s[6:7], -1, 0
	s_waitcnt lgkmcnt(0)
	v_cmp_lt_u32_e32 vcc, s34, v200
	s_or_b64 s[6:7], vcc, s[6:7]
	s_andn2_b64 vcc, exec, s[6:7]
	s_cbranch_vccz .LBB0_2195
	v_mov_b32_e32 v200, s28
	s_sleep 2
	ds_read_b32 v200, v200
	s_add_i32 s30, s30, -8
	s_waitcnt lgkmcnt(0)
	v_cmp_lt_u32_e64 s[22:23], s34, v200
	s_branch .LBB0_2195

.LBB0_2841:
	s_waitcnt lgkmcnt(0)
	v_dot8_i32_i4 v39, v8, v0, 0
	v_dot8_i32_i4 v41, v10, v0, 0
	v_dot8_i32_i4 v40, v14, v0, 0
	v_dot8_i32_i4 v42, v20, v0, 0
	v_dot8_i32_i4 v35, v8, v2, 0
	v_dot8_i32_i4 v36, v10, v2, 0
	v_dot8_i32_i4 v37, v14, v2, 0
	v_dot8_i32_i4 v38, v20, v2, 0
	v_dot8_i32_i4 v39, v9, v1, v39
	v_dot8_i32_i4 v41, v11, v1, v41
	v_dot8_i32_i4 v40, v15, v1, v40
	v_dot8_i32_i4 v42, v21, v1, v42
	v_dot8_i32_i4 v35, v9, v3, v35
	v_dot8_i32_i4 v36, v11, v3, v36
	v_dot8_i32_i4 v37, v15, v3, v37
	v_dot8_i32_i4 v38, v21, v3, v38
	v_lshl_add_u32 v39, v39, 4, v35
	v_lshl_add_u32 v41, v41, 4, v36
	v_lshl_add_u32 v40, v40, 4, v37
	v_lshl_add_u32 v42, v42, 4, v38
	s_nop 1
	s_mulk_i32 s1, 0x690
	v_permlane32_swap_b32_e32 v39, v40
	v_permlane32_swap_b32_e32 v41, v42
	v_add_u32_e32 v8, v39, v40
	v_add_u32_e32 v9, v41, v42
	s_nop 1
	v_permlane16_swap_b32_e32 v8, v9
	v_add_u32_e32 v8, v8, v9
	s_lshr_b32 s4, s10, 17
	s_add_i32 s1, s90, s1
	v_add_u32_dpp v8, v8, v8 quad_perm:[1,0,3,2] row_mask:0xf bank_mask:0xf bound_ctrl:1
	s_and_b32 s4, s4, 0x7ffc
	s_add_i32 s1, s1, s4
	v_add_u32_dpp v8, v8, v8 quad_perm:[2,3,0,1] row_mask:0xf bank_mask:0xf bound_ctrl:1
	v_lshl_add_u32 v34, v33, 2, s1
	v_add_u32_dpp v9, v8, v8 row_half_mirror row_mask:0xf bank_mask:0xf bound_ctrl:1
	s_nop 1
	v_mov_b32_dpp v10, v9 row_mirror row_mask:0xf bank_mask:0xf bound_ctrl:1
	v_add_u32_e32 v10, v9, v10
	s_and_saveexec_b64 s[0:1], vcc
	ds_write_b32 v34, v10
	s_or_b64 exec, exec, s[0:1]

.LBB0_2849:
	s_waitcnt lgkmcnt(0)
	v_dot8_i32_i4 v39, v12, v0, 0
	v_dot8_i32_i4 v41, v18, v0, 0
	v_dot8_i32_i4 v40, v24, v0, 0
	v_dot8_i32_i4 v42, v26, v0, 0
	v_dot8_i32_i4 v35, v12, v2, 0
	v_dot8_i32_i4 v36, v18, v2, 0
	v_dot8_i32_i4 v37, v24, v2, 0
	v_dot8_i32_i4 v38, v26, v2, 0
	v_dot8_i32_i4 v39, v13, v1, v39
	v_dot8_i32_i4 v41, v19, v1, v41
	v_dot8_i32_i4 v40, v25, v1, v40
	v_dot8_i32_i4 v42, v27, v1, v42
	v_dot8_i32_i4 v35, v13, v3, v35
	v_dot8_i32_i4 v36, v19, v3, v36
	v_dot8_i32_i4 v37, v25, v3, v37
	v_dot8_i32_i4 v38, v27, v3, v38
	v_lshl_add_u32 v39, v39, 4, v35
	v_lshl_add_u32 v41, v41, 4, v36
	v_lshl_add_u32 v40, v40, 4, v37
	v_lshl_add_u32 v42, v42, 4, v38
	s_nop 1
	s_mulk_i32 s1, 0x690
	v_permlane32_swap_b32_e32 v39, v40
	v_permlane32_swap_b32_e32 v41, v42
	v_add_u32_e32 v12, v39, v40
	v_add_u32_e32 v13, v41, v42
	s_nop 1
	v_permlane16_swap_b32_e32 v12, v13
	v_add_u32_e32 v12, v12, v13
	s_lshr_b32 s4, s11, 17
	s_add_i32 s1, s90, s1
	v_add_u32_dpp v12, v12, v12 quad_perm:[1,0,3,2] row_mask:0xf bank_mask:0xf bound_ctrl:1
	s_and_b32 s4, s4, 0x7ffc
	s_add_i32 s1, s1, s4
	v_add_u32_dpp v12, v12, v12 quad_perm:[2,3,0,1] row_mask:0xf bank_mask:0xf bound_ctrl:1
	v_lshl_add_u32 v34, v33, 2, s1
	v_add_u32_dpp v13, v12, v12 row_half_mirror row_mask:0xf bank_mask:0xf bound_ctrl:1
	s_nop 1
	v_mov_b32_dpp v18, v13 row_mirror row_mask:0xf bank_mask:0xf bound_ctrl:1
	v_add_u32_e32 v18, v13, v18
	s_and_saveexec_b64 s[0:1], vcc
	ds_write_b32 v34, v18
	s_or_b64 exec, exec, s[0:1]

; #define LAS __attribute__((address_space(3)))
;     ...
;     float wsj[PE_NT];
; #pragma unroll
;     for (int j = 0; j < PE_NT; ++j) {
;         LAS unsigned* lt = lw + j * PE_TOK_W + 128;
;         const float a0 = __builtin_bit_cast(float, lt[2 * lane]), a1 = __builtin_bit_cast(float, lt[2 * lane + 1]);
;         const float wm = fmaxf(wave_max(fmaxf(fabsf(a0), fabsf(a1))), 1e-30f), wq = 127.0f * __builtin_amdgcn_rcpf(wm);
;         wsj[j] = wm * (1.0f / 127.0f);
;         const unsigned pr = (__builtin_bit_cast(unsigned, __builtin_fmaf(a0, wq, 12582912.0f)) & 0xffu) | ((__builtin_bit_cast(unsigned, __builtin_fmaf(a1, wq, 12582912.0f)) & 0xffu) << 8);
;         const unsigned nbp = (unsigned)__builtin_amdgcn_update_dpp(0, (int)pr, 0xB1, 0xF, 0xF, true);
;         asm volatile("" ::: "memory");
;         if ((lane & 1) == 0) lt[2 * lane] = pr | (nbp << 16);
;     }
.LBB0_2857:
	s_waitcnt lgkmcnt(0)
	v_dot8_i32_i4 v39, v16, v0, 0
	v_dot8_i32_i4 v41, v22, v0, 0
	v_dot8_i32_i4 v40, v28, v0, 0
	v_dot8_i32_i4 v42, v30, v0, 0
	v_dot8_i32_i4 v35, v16, v2, 0
	v_dot8_i32_i4 v36, v22, v2, 0
	v_dot8_i32_i4 v37, v28, v2, 0
	v_dot8_i32_i4 v38, v30, v2, 0
	v_dot8_i32_i4 v39, v17, v1, v39
	v_dot8_i32_i4 v41, v23, v1, v41
	v_dot8_i32_i4 v40, v29, v1, v40
	v_dot8_i32_i4 v42, v31, v1, v42
	v_dot8_i32_i4 v35, v17, v3, v35
	v_dot8_i32_i4 v36, v23, v3, v36
	v_dot8_i32_i4 v37, v29, v3, v37
	v_dot8_i32_i4 v38, v31, v3, v38
	v_lshl_add_u32 v39, v39, 4, v35
	v_lshl_add_u32 v41, v41, 4, v36
	v_lshl_add_u32 v40, v40, 4, v37
	v_lshl_add_u32 v42, v42, 4, v38
	s_nop 1
	s_mulk_i32 s1, 0x690
	v_permlane32_swap_b32_e32 v39, v40
	v_permlane32_swap_b32_e32 v41, v42
	v_add_u32_e32 v16, v39, v40
	v_add_u32_e32 v17, v41, v42
	s_nop 1
	v_permlane16_swap_b32_e32 v16, v17
	v_add_u32_e32 v16, v16, v17
	s_lshr_b32 s4, s12, 17
	s_add_i32 s1, s90, s1
	v_add_u32_dpp v16, v16, v16 quad_perm:[1,0,3,2] row_mask:0xf bank_mask:0xf bound_ctrl:1
	s_and_b32 s4, s4, 0x7ffc
	s_add_i32 s1, s1, s4
	v_add_u32_dpp v16, v16, v16 quad_perm:[2,3,0,1] row_mask:0xf bank_mask:0xf bound_ctrl:1
	v_lshl_add_u32 v34, v33, 2, s1
	v_add_u32_dpp v17, v16, v16 row_half_mirror row_mask:0xf bank_mask:0xf bound_ctrl:1
	s_nop 1
	v_mov_b32_dpp v22, v17 row_mirror row_mask:0xf bank_mask:0xf bound_ctrl:1
	v_add_u32_e32 v22, v17, v22
	s_and_saveexec_b64 s[0:1], vcc
	ds_write_b32 v34, v22
	s_branch .LBB0_2836
.LBB0_2861:
	s_waitcnt vmcnt(0)
	s_waitcnt vmcnt(0)
	s_waitcnt vmcnt(0)
	s_waitcnt lgkmcnt(0)
	v_add_u32_e32 v1, s90, v118
	ds_read_b64 v[126:127], v1
	ds_read_b64 v[128:129], v1 offset:1024
	ds_read_b64 v[2:3], v1 offset:512
	s_mov_b32 s0, 0xc0c0500
	v_and_b32_e32 v5, 1, v50
	v_cmp_eq_u32_e32 vcc, 0, v5
	s_waitcnt lgkmcnt(0)
	v_cvt_f32_i32_e32 v126, v126
	v_cvt_f32_i32_e32 v127, v127
	v_mul_f32_e32 v126, v128, v126
	v_mul_f32_e32 v127, v129, v127
	v_mul_f32_e32 v94, v126, v126
	v_mul_f32_e32 v95, v127, v127
	v_fmamk_f32 v94, v94, 0xbdd2d3e8, v113
	v_fmamk_f32 v95, v95, 0xbdd2d3e8, v113
	v_mul_f32_e32 v94, v126, v94
	v_mul_f32_e32 v95, v127, v95
	v_exp_f32_e32 v94, v94
	v_exp_f32_e32 v95, v95
	s_nop 0
	v_add_f32_e32 v94, 1.0, v94
	v_add_f32_e32 v95, 1.0, v95
	v_rcp_f32_e32 v94, v94
	v_rcp_f32_e32 v95, v95
	s_nop 0
	v_mul_f32_e32 v126, v126, v94
	v_mul_f32_e32 v127, v127, v95
	v_mul_f32_e32 v2, v2, v126
	v_mul_f32_e32 v3, v3, v127
	v_max_f32_e64 v0, |v3|, |v3|
	v_max_f32_e64 v4, |v2|, |v2|
	v_max_f32_e32 v0, v4, v0
	s_nop 1
	v_mov_b32_dpp v4, v0 quad_perm:[1,0,3,2] row_mask:0xf bank_mask:0xf bound_ctrl:1
	v_max_f32_e32 v4, v4, v4
	v_max_f32_e32 v0, v0, v4
	s_nop 1
	v_mov_b32_dpp v4, v0 quad_perm:[2,3,0,1] row_mask:0xf bank_mask:0xf bound_ctrl:1
	v_max_f32_e32 v4, v4, v4
	v_max_f32_e32 v0, v0, v4
	s_nop 1
	v_mov_b32_dpp v4, v0 row_half_mirror row_mask:0xf bank_mask:0xf bound_ctrl:1
	v_max_f32_e32 v4, v4, v4
	v_max_f32_e32 v0, v0, v4
	s_nop 1
	v_mov_b32_dpp v4, v0 row_mirror row_mask:0xf bank_mask:0xf bound_ctrl:1
	v_max_f32_e32 v4, v4, v4
	v_max_f32_e32 v0, v0, v4
	v_mov_b32_e32 v4, v0
	s_nop 1
	v_permlane16_swap_b32_e32 v0, v4
	v_max_f32 v0, v0, v4
	s_nop 1
	s_nop 0
	v_mov_b32_e32 v4, v0
	s_nop 1
	v_permlane32_swap_b32_e32 v0, v4
	v_max_f32 v0, v0, v4
	s_nop 0
	v_max_f32_e32 v0, v0, v0
	v_max_f32_e32 v0, 0xda24260, v0
	v_rcp_f32_e32 v4, v0
	s_nop 0
	v_mul_f32_e32 v4, 0x42fe0000, v4
	v_fmaak_f32 v3, v3, v4, 0x4b400000
	v_fmaak_f32 v2, v2, v4, 0x4b400000
	v_lshlrev_b32_e32 v3, 8, v3
	v_perm_b32 v2, v3, v2, s0
	s_nop 1
	v_mov_b32_dpp v3, v2 quad_perm:[1,0,3,2] row_mask:0xf bank_mask:0xf bound_ctrl:1
	s_and_saveexec_b64 s[0:1], vcc
	v_lshl_or_b32 v2, v3, 16, v2
	ds_write_b32 v1, v2 offset:512
	s_or_b64 exec, exec, s[0:1]
	ds_read_b64 v[126:127], v1 offset:1680
	ds_read_b64 v[128:129], v1 offset:2704
	ds_read_b64 v[4:5], v1 offset:2192
	s_mov_b32 s0, 0xc0c0500
	s_waitcnt lgkmcnt(0)
	v_cvt_f32_i32_e32 v126, v126
	v_cvt_f32_i32_e32 v127, v127
	v_mul_f32_e32 v126, v128, v126
	v_mul_f32_e32 v127, v129, v127
	v_mul_f32_e32 v94, v126, v126
	v_mul_f32_e32 v95, v127, v127
	v_fmamk_f32 v94, v94, 0xbdd2d3e8, v113
	v_fmamk_f32 v95, v95, 0xbdd2d3e8, v113
	v_mul_f32_e32 v94, v126, v94
	v_mul_f32_e32 v95, v127, v95
	v_exp_f32_e32 v94, v94
	v_exp_f32_e32 v95, v95
	s_nop 0
	v_add_f32_e32 v94, 1.0, v94
	v_add_f32_e32 v95, 1.0, v95
	v_rcp_f32_e32 v94, v94
	v_rcp_f32_e32 v95, v95
	s_nop 0
	v_mul_f32_e32 v126, v126, v94
	v_mul_f32_e32 v127, v127, v95
	v_mul_f32_e32 v4, v4, v126
	v_mul_f32_e32 v5, v5, v127
	v_max_f32_e64 v2, |v5|, |v5|
	v_max_f32_e64 v3, |v4|, |v4|
	v_max_f32_e32 v2, v3, v2
	s_nop 1
	v_mov_b32_dpp v3, v2 quad_perm:[1,0,3,2] row_mask:0xf bank_mask:0xf bound_ctrl:1
	v_max_f32_e32 v3, v3, v3
	v_max_f32_e32 v2, v2, v3
	s_nop 1
	v_mov_b32_dpp v3, v2 quad_perm:[2,3,0,1] row_mask:0xf bank_mask:0xf bound_ctrl:1
	v_max_f32_e32 v3, v3, v3
	v_max_f32_e32 v2, v2, v3
	s_nop 1
	v_mov_b32_dpp v3, v2 row_half_mirror row_mask:0xf bank_mask:0xf bound_ctrl:1
	v_max_f32_e32 v3, v3, v3
	v_max_f32_e32 v2, v2, v3
	s_nop 1
	v_mov_b32_dpp v3, v2 row_mirror row_mask:0xf bank_mask:0xf bound_ctrl:1
	v_max_f32_e32 v3, v3, v3
	v_max_f32_e32 v2, v2, v3
	v_mov_b32_e32 v3, v2
	s_nop 1
	v_permlane16_swap_b32_e32 v2, v3
	v_max_f32 v2, v2, v3
	s_nop 1
	s_nop 0
	v_mov_b32_e32 v3, v2
	s_nop 1
	v_permlane32_swap_b32_e32 v2, v3
	v_max_f32 v2, v2, v3
	s_nop 0
	v_max_f32_e32 v2, v2, v2
	v_max_f32_e32 v2, 0xda24260, v2
	v_rcp_f32_e32 v3, v2
	s_nop 0
	v_mul_f32_e32 v3, 0x42fe0000, v3
	v_fmaak_f32 v4, v4, v3, 0x4b400000
	v_fmaak_f32 v3, v5, v3, 0x4b400000
	v_lshlrev_b32_e32 v3, 8, v3
	v_perm_b32 v3, v3, v4, s0
	s_nop 1
	v_mov_b32_dpp v4, v3 quad_perm:[1,0,3,2] row_mask:0xf bank_mask:0xf bound_ctrl:1
	s_and_saveexec_b64 s[0:1], vcc
	v_lshl_or_b32 v3, v4, 16, v3
	ds_write_b32 v1, v3 offset:2192
	s_or_b64 exec, exec, s[0:1]
	ds_read_b64 v[126:127], v1 offset:3360
	ds_read_b64 v[128:129], v1 offset:4384
	ds_read_b64 v[4:5], v1 offset:3872
	s_mov_b32 s0, 0xc0c0500
	s_waitcnt lgkmcnt(0)
; #define LAS __attribute__((address_space(3)))
; #define LDS_WAIT() asm volatile("s_waitcnt lgkmcnt(0)" ::: "memory")
;     ...
;     float wsj[PE_NT];
; #pragma unroll
;     for (int j = 0; j < PE_NT; ++j) {
;         LAS unsigned* lt = lw + j * PE_TOK_W + 128;
;         const float a0 = __builtin_bit_cast(float, lt[2 * lane]), a1 = __builtin_bit_cast(float, lt[2 * lane + 1]);
;         const float wm = fmaxf(wave_max(fmaxf(fabsf(a0), fabsf(a1))), 1e-30f), wq = 127.0f * __builtin_amdgcn_rcpf(wm);
;         wsj[j] = wm * (1.0f / 127.0f);
;         const unsigned pr = (__builtin_bit_cast(unsigned, __builtin_fmaf(a0, wq, 12582912.0f)) & 0xffu) | ((__builtin_bit_cast(unsigned, __builtin_fmaf(a1, wq, 12582912.0f)) & 0xffu) << 8);
;         const unsigned nbp = (unsigned)__builtin_amdgcn_update_dpp(0, (int)pr, 0xB1, 0xF, 0xF, true);
;         asm volatile("" ::: "memory");
;         if ((lane & 1) == 0) lt[2 * lane] = pr | (nbp << 16);
;     }
;     LDS_WAIT(); asm volatile("" ::: "memory");
;     {
;         unsigned er[PE_RD];
; #pragma unroll
;         for (int q = 0; q < PE_RD; ++q) { const v4u rec = *(const LAS v4u*)(ents + 4 * q); er[q] = __builtin_amdgcn_readfirstlane(rec.x); PE_ISSUE4(q, rec, VB8); }
;         int curi[16];
; #pragma unroll
;         for (int i = 0; i < 16; ++i) curi[i] = 0;
;         int jcur = (int)((er[0] >> 14) & 3u);
;         v4u nrec = *(const LAS v4u*)(ents + 4 * PE_RD);
	v_cvt_f32_i32_e32 v126, v126
	v_cvt_f32_i32_e32 v127, v127
	v_mul_f32_e32 v126, v128, v126
	v_mul_f32_e32 v127, v129, v127
	v_mul_f32_e32 v94, v126, v126
	v_mul_f32_e32 v95, v127, v127
	v_fmamk_f32 v94, v94, 0xbdd2d3e8, v113
	v_fmamk_f32 v95, v95, 0xbdd2d3e8, v113
	v_mul_f32_e32 v94, v126, v94
	v_mul_f32_e32 v95, v127, v95
	v_exp_f32_e32 v94, v94
	v_exp_f32_e32 v95, v95
	s_nop 0
	v_add_f32_e32 v94, 1.0, v94
	v_add_f32_e32 v95, 1.0, v95
	v_rcp_f32_e32 v94, v94
	v_rcp_f32_e32 v95, v95
	s_nop 0
	v_mul_f32_e32 v126, v126, v94
	v_mul_f32_e32 v127, v127, v95
	v_mul_f32_e32 v4, v4, v126
	v_mul_f32_e32 v5, v5, v127
	v_max_f32_e64 v3, |v5|, |v5|
	v_max_f32_e64 v6, |v4|, |v4|
	v_max_f32_e32 v3, v6, v3
	s_nop 1
	v_mov_b32_dpp v6, v3 quad_perm:[1,0,3,2] row_mask:0xf bank_mask:0xf bound_ctrl:1
	v_max_f32_e32 v6, v6, v6
	v_max_f32_e32 v3, v3, v6
	s_nop 1
	v_mov_b32_dpp v6, v3 quad_perm:[2,3,0,1] row_mask:0xf bank_mask:0xf bound_ctrl:1
	v_max_f32_e32 v6, v6, v6
	v_max_f32_e32 v3, v3, v6
	s_nop 1
	v_mov_b32_dpp v6, v3 row_half_mirror row_mask:0xf bank_mask:0xf bound_ctrl:1
	v_max_f32_e32 v6, v6, v6
	v_max_f32_e32 v3, v3, v6
	s_nop 1
	v_mov_b32_dpp v6, v3 row_mirror row_mask:0xf bank_mask:0xf bound_ctrl:1
	v_max_f32_e32 v6, v6, v6
	v_max_f32_e32 v3, v3, v6
	v_mov_b32_e32 v6, v3
	s_nop 1
	v_permlane16_swap_b32_e32 v3, v6
	v_max_f32 v3, v3, v6
	s_nop 1
	s_nop 0
	v_mov_b32_e32 v6, v3
	s_nop 1
	v_permlane32_swap_b32_e32 v3, v6
	v_max_f32 v3, v3, v6
	s_nop 0
	v_max_f32_e32 v3, v3, v3
	v_max_f32_e32 v3, 0xda24260, v3
	v_rcp_f32_e32 v6, v3
	s_nop 0
	v_mul_f32_e32 v6, 0x42fe0000, v6
	v_fmaak_f32 v5, v5, v6, 0x4b400000
	v_fmaak_f32 v4, v4, v6, 0x4b400000
	v_lshlrev_b32_e32 v5, 8, v5
	v_perm_b32 v4, v5, v4, s0
	s_nop 1
	v_mov_b32_dpp v5, v4 quad_perm:[1,0,3,2] row_mask:0xf bank_mask:0xf bound_ctrl:1
	s_and_saveexec_b64 s[0:1], vcc
	v_lshl_or_b32 v4, v5, 16, v4
	ds_write_b32 v1, v4 offset:3872
	s_or_b64 exec, exec, s[0:1]
	ds_read_b64 v[126:127], v1 offset:5040
	ds_read_b64 v[128:129], v1 offset:6064
	ds_read_b64 v[6:7], v1 offset:5552
	s_mov_b32 s0, 0xc0c0500
	s_waitcnt lgkmcnt(0)
	v_cvt_f32_i32_e32 v126, v126
	v_cvt_f32_i32_e32 v127, v127
	v_mul_f32_e32 v126, v128, v126
	v_mul_f32_e32 v127, v129, v127
	v_mul_f32_e32 v94, v126, v126
	v_mul_f32_e32 v95, v127, v127
	v_fmamk_f32 v94, v94, 0xbdd2d3e8, v113
	v_fmamk_f32 v95, v95, 0xbdd2d3e8, v113
	v_mul_f32_e32 v94, v126, v94
	v_mul_f32_e32 v95, v127, v95
	v_exp_f32_e32 v94, v94
	v_exp_f32_e32 v95, v95
	s_nop 0
	v_add_f32_e32 v94, 1.0, v94
	v_add_f32_e32 v95, 1.0, v95
	v_rcp_f32_e32 v94, v94
	v_rcp_f32_e32 v95, v95
	s_nop 0
	v_mul_f32_e32 v126, v126, v94
	v_mul_f32_e32 v127, v127, v95
	v_mul_f32_e32 v6, v6, v126
	v_mul_f32_e32 v7, v7, v127
	v_max_f32_e64 v4, |v7|, |v7|
	v_max_f32_e64 v5, |v6|, |v6|
	v_max_f32_e32 v4, v5, v4
	s_nop 1
	v_mov_b32_dpp v5, v4 quad_perm:[1,0,3,2] row_mask:0xf bank_mask:0xf bound_ctrl:1
	v_max_f32_e32 v5, v5, v5
	v_max_f32_e32 v4, v4, v5
	s_nop 1
	v_mov_b32_dpp v5, v4 quad_perm:[2,3,0,1] row_mask:0xf bank_mask:0xf bound_ctrl:1
	v_max_f32_e32 v5, v5, v5
	v_max_f32_e32 v4, v4, v5
	s_nop 1
	v_mov_b32_dpp v5, v4 row_half_mirror row_mask:0xf bank_mask:0xf bound_ctrl:1
	v_max_f32_e32 v5, v5, v5
	v_max_f32_e32 v4, v4, v5
	s_nop 1
	v_mov_b32_dpp v5, v4 row_mirror row_mask:0xf bank_mask:0xf bound_ctrl:1
	v_max_f32_e32 v5, v5, v5
	v_max_f32_e32 v4, v4, v5
	v_mov_b32_e32 v5, v4
	s_nop 1
	v_permlane16_swap_b32_e32 v4, v5
	v_max_f32 v4, v4, v5
	s_nop 1
	s_nop 0
	v_mov_b32_e32 v5, v4
	s_nop 1
	v_permlane32_swap_b32_e32 v4, v5
	v_max_f32 v4, v4, v5
	s_nop 0
	v_max_f32_e32 v4, v4, v4
	v_max_f32_e32 v4, 0xda24260, v4
	v_rcp_f32_e32 v5, v4
	s_nop 0
	v_mul_f32_e32 v5, 0x42fe0000, v5
	v_fmaak_f32 v6, v6, v5, 0x4b400000
	v_fmaak_f32 v5, v7, v5, 0x4b400000
	v_lshlrev_b32_e32 v5, 8, v5
	v_perm_b32 v5, v5, v6, s0
	s_nop 1
	v_mov_b32_dpp v6, v5 quad_perm:[1,0,3,2] row_mask:0xf bank_mask:0xf bound_ctrl:1
	s_and_saveexec_b64 s[0:1], vcc
	v_lshl_or_b32 v5, v6, 16, v5
	ds_write_b32 v1, v5 offset:5552
	s_or_b64 exec, exec, s[0:1]
	s_waitcnt lgkmcnt(0)
	v_mov_b32_e32 v1, s90
	ds_read_b128 v[6:9], v1 offset:6720
	v_mul_f32_e32 v119, 0x3c010204, v3
	v_mul_f32_e32 v117, 0x3c010204, v4
	v_mul_f32_e32 v121, 0x3c010204, v0
	v_mul_f32_e32 v120, 0x3c010204, v2
	s_waitcnt lgkmcnt(0)
	v_lshlrev_b32_e32 v5, 9, v6
	v_and_b32_e32 v5, 0x7ffe00, v5
	v_add_u32_e32 v5, v5, v118
	global_load_dwordx2 v[70:71], v5, s[82:83]
	v_lshl_add_u32 v7, v7, 9, v118
	global_load_dwordx2 v[72:73], v7, s[82:83]
	v_lshl_add_u32 v8, v8, 9, v118
	global_load_dwordx2 v[74:75], v8, s[82:83]
	v_lshl_add_u32 v9, v9, 9, v118
	global_load_dwordx2 v[80:81], v9, s[82:83]
	ds_read_b128 v[8:11], v1 offset:6736
	v_readfirstlane_b32 s4, v6
	s_bfe_u32 s7, s4, 0x2000e
	s_andn2_b64 vcc, exec, s[2:3]
	s_mov_b32 s0, 0
	s_waitcnt lgkmcnt(0)
	v_lshlrev_b32_e32 v3, 9, v8
	v_and_b32_e32 v3, 0x7ffe00, v3
	v_add_u32_e32 v3, v3, v118
	global_load_dwordx2 v[76:77], v3, s[82:83]
	v_lshl_add_u32 v4, v9, 9, v118
	global_load_dwordx2 v[82:83], v4, s[82:83]
	v_lshl_add_u32 v5, v10, 9, v118
	global_load_dwordx2 v[84:85], v5, s[82:83]
	v_lshl_add_u32 v3, v11, 9, v118
	global_load_dwordx2 v[90:91], v3, s[82:83]
	ds_read_b128 v[10:13], v1 offset:6752
	v_readfirstlane_b32 s5, v8
	s_waitcnt lgkmcnt(0)
	v_lshlrev_b32_e32 v0, 9, v10
	v_and_b32_e32 v0, 0x7ffe00, v0
	v_add_u32_e32 v0, v0, v118
	global_load_dwordx2 v[78:79], v0, s[82:83]
	v_lshl_add_u32 v0, v11, 9, v118
	global_load_dwordx2 v[86:87], v0, s[82:83]
	v_lshl_add_u32 v0, v12, 9, v118
	global_load_dwordx2 v[88:89], v0, s[82:83]
	v_lshl_add_u32 v0, v13, 9, v118
	global_load_dwordx2 v[92:93], v0, s[82:83]
	v_readfirstlane_b32 s8, v10
	s_cbranch_vccnz .LBB0_2884
; #define LAS __attribute__((address_space(3)))
;     ...
;         for (int i = 0; i < 8; ++i) acc[j][i] = (f32x2){0.f, 0.f};
;     ...
;         int curi[16];
; #pragma unroll
;         for (int i = 0; i < 16; ++i) curi[i] = 0;
;         int jcur = (int)((er[0] >> 14) & 3u);
;         v4u nrec = *(const LAS v4u*)(ents + 4 * PE_RD);
	v_mov_b32_e32 v48, v49
	v_mov_b32_e32 v94, 0
	v_mov_b32_e32 v95, 0
	v_mov_b32_e32 v96, 0
	v_mov_b32_e32 v97, 0
	v_mov_b32_e32 v98, 0
	v_mov_b32_e32 v99, 0
	v_mov_b32_e32 v100, 0
	v_mov_b32_e32 v101, 0
	v_mov_b32_e32 v102, 0
	v_mov_b32_e32 v103, 0
	v_mov_b32_e32 v104, 0
	v_mov_b32_e32 v105, 0
	v_mov_b32_e32 v106, 0
	v_mov_b32_e32 v107, 0
	v_mov_b32_e32 v108, 0
	v_mov_b32_e32 v109, 0
	v_readlane_b32 s1, v255, 2
	v_mov_b64_e32 v[12:13], v[48:49]
	v_mov_b64_e32 v[14:15], v[48:49]
	v_mov_b64_e32 v[16:17], v[48:49]
	v_mov_b64_e32 v[18:19], v[48:49]
	v_mov_b64_e32 v[34:35], v[48:49]
	v_mov_b64_e32 v[32:33], v[48:49]
	v_mov_b64_e32 v[30:31], v[48:49]
	v_mov_b64_e32 v[28:29], v[48:49]
	v_mov_b64_e32 v[26:27], v[48:49]
	v_mov_b64_e32 v[24:25], v[48:49]
	v_mov_b64_e32 v[22:23], v[48:49]
	v_mov_b64_e32 v[20:21], v[48:49]
	v_mov_b64_e32 v[52:53], v[48:49]
	v_mov_b64_e32 v[50:51], v[48:49]
	v_mov_b64_e32 v[46:47], v[48:49]
	v_mov_b64_e32 v[44:45], v[48:49]
	v_mov_b64_e32 v[42:43], v[48:49]
	v_mov_b64_e32 v[40:41], v[48:49]
	v_mov_b64_e32 v[38:39], v[48:49]
	v_mov_b64_e32 v[36:37], v[48:49]
	v_mov_b64_e32 v[68:69], v[48:49]
	v_mov_b64_e32 v[66:67], v[48:49]
	v_mov_b64_e32 v[64:65], v[48:49]
	v_mov_b64_e32 v[62:63], v[48:49]
	v_mov_b64_e32 v[60:61], v[48:49]
	v_mov_b64_e32 v[58:59], v[48:49]
	v_mov_b64_e32 v[56:57], v[48:49]
	v_mov_b64_e32 v[54:55], v[48:49]
	v_mov_b64_e32 v[10:11], v[48:49]
	v_mov_b64_e32 v[8:9], v[48:49]
	v_mov_b64_e32 v[6:7], v[48:49]
	v_mov_b64_e32 v[4:5], v[48:49]
	s_branch .LBB0_2873
